# weight-conversion loop: the 8 waves of a workgroup re-synchronised every item (s_barrier at loop head) so their row loads hit the same DRAM pages together
# speedup vs baseline: 1.0036x; 1.0036x over previous
.LBB0_25:
	s_barrier
	v_add_u32_e32 v66, s35, v134
	v_mad_i64_i32 v[66:67], s[0:1], v66, s92, 0
	v_lshl_add_u64 v[66:67], v[66:67], 2, s[82:83]
	s_ashr_i32 s85, s84, 31
	s_ashr_i32 s93, s92, 31
	v_lshl_add_u64 v[66:67], s[84:85], 2, v[66:67]
	v_lshl_add_u64 v[66:67], v[66:67], 0, v[136:137]
	s_lshl_b64 s[0:1], s[92:93], 4
	v_lshl_add_u64 v[68:69], v[66:67], 0, s[0:1]
	v_lshl_add_u64 v[74:75], v[68:69], 0, s[0:1]
	global_load_dwordx4 v[114:117], v[66:67], off nt
	global_load_dwordx4 v[70:73], v[68:69], off nt
	v_lshl_add_u64 v[66:67], v[74:75], 0, s[0:1]
	v_lshl_add_u64 v[68:69], v[66:67], 0, s[0:1]
	global_load_dwordx4 v[118:121], v[74:75], off nt
	s_nop 0
	global_load_dwordx4 v[74:77], v[66:67], off nt
	v_lshl_add_u64 v[66:67], v[68:69], 0, s[0:1]
	v_lshl_add_u64 v[82:83], v[66:67], 0, s[0:1]
	global_load_dwordx4 v[122:125], v[68:69], off nt
	global_load_dwordx4 v[78:81], v[66:67], off nt
	v_lshl_add_u64 v[66:67], v[82:83], 0, s[0:1]
	v_lshl_add_u64 v[68:69], v[66:67], 0, s[0:1]
	global_load_dwordx4 v[126:129], v[82:83], off nt
	s_nop 0
	global_load_dwordx4 v[82:85], v[66:67], off nt
	v_lshl_add_u64 v[66:67], v[68:69], 0, s[0:1]
	global_load_dwordx4 v[86:89], v[68:69], off nt
	v_lshl_add_u64 v[68:69], v[66:67], 0, s[0:1]
	global_load_dwordx4 v[90:93], v[66:67], off nt
	v_lshl_add_u64 v[66:67], v[68:69], 0, s[0:1]
	global_load_dwordx4 v[94:97], v[68:69], off nt
	v_lshl_add_u64 v[68:69], v[66:67], 0, s[0:1]
	global_load_dwordx4 v[98:101], v[66:67], off nt
	v_lshl_add_u64 v[66:67], v[68:69], 0, s[0:1]
	global_load_dwordx4 v[102:105], v[68:69], off nt
	v_lshl_add_u64 v[68:69], v[66:67], 0, s[0:1]
	global_load_dwordx4 v[106:109], v[66:67], off nt
	v_lshl_add_u64 v[66:67], v[68:69], 0, s[0:1]
	global_load_dwordx4 v[110:113], v[68:69], off nt
	s_nop 0
	global_load_dwordx4 v[66:69], v[66:67], off nt
	v_add_u32_e32 v178, 0x410, v170
	v_add_u32_e32 v179, 0x418, v170
	v_add_u32_e32 v180, 0x820, v170
	v_add_u32_e32 v181, 0x828, v170
	v_add_u32_e32 v182, 0xc30, v170
	v_add_u32_e32 v183, 0xc38, v170
	v_add_u32_e32 v184, 0x1040, v170
	v_add_u32_e32 v185, 0x1048, v170
	v_add_u32_e32 v186, 0x1450, v170
	v_add_u32_e32 v187, 0x1458, v170
	v_add_u32_e32 v188, 0x1860, v170
	v_add_u32_e32 v189, 0x1868, v170
	v_add_u32_e32 v190, 0x1c70, v170
	v_add_u32_e32 v191, 0x1c78, v170
	v_add_u32_e32 v192, 0x2080, v170
	v_add_u32_e32 v193, 0x2088, v170
	v_add_u32_e32 v194, 0x2490, v170
	v_add_u32_e32 v195, 0x2498, v170
	v_add_u32_e32 v196, 0x28a0, v170
	v_add_u32_e32 v197, 0x28a8, v170
	v_add_u32_e32 v198, 0x2cb0, v170
	v_add_u32_e32 v199, 0x2cb8, v170
	v_add_u32_e32 v200, 0x30c0, v170
	v_add_u32_e32 v201, 0x30c8, v170
	v_add_u32_e32 v202, 0x34d0, v170
	v_add_u32_e32 v203, 0x34d8, v170
	v_add_u32_e32 v204, 0x38e0, v170
	v_add_u32_e32 v205, 0x38e8, v170
	v_add_u32_e32 v206, 0x3cf0, v170
	v_add_u32_e32 v207, 0x3cf8, v170
	s_waitcnt vmcnt(16)
	ds_write2_b32 v170, v42, v43 offset1:1
	ds_write2_b32 v170, v44, v45 offset0:2 offset1:3
	ds_write2_b32 v178, v38, v39 offset1:1
	ds_write2_b32 v179, v40, v41 offset1:1
	ds_write2_b32 v180, v50, v51 offset1:1
	ds_write2_b32 v181, v52, v53 offset1:1
	ds_write2_b32 v182, v46, v47 offset1:1
	ds_write2_b32 v183, v48, v49 offset1:1
	ds_write2_b32 v184, v58, v59 offset1:1
	ds_write2_b32 v185, v60, v61 offset1:1
	ds_write2_b32 v186, v54, v55 offset1:1
	ds_write2_b32 v187, v56, v57 offset1:1
	ds_write2_b32 v188, v34, v35 offset1:1
	ds_write2_b32 v189, v36, v37 offset1:1
	ds_write2_b32 v190, v14, v15 offset1:1
	ds_write2_b32 v191, v16, v17 offset1:1
	ds_write2_b32 v192, v18, v19 offset1:1
	ds_write2_b32 v193, v20, v21 offset1:1
	ds_write2_b32 v194, v22, v23 offset1:1
	ds_write2_b32 v195, v24, v25 offset1:1
	ds_write2_b32 v196, v30, v31 offset1:1
	ds_write2_b32 v197, v32, v33 offset1:1
	ds_write2_b32 v198, v6, v7 offset1:1
	ds_write2_b32 v199, v8, v9 offset1:1
	ds_write2_b32 v200, v26, v27 offset1:1
	ds_write2_b32 v201, v28, v29 offset1:1
	ds_write2_b32 v202, v2, v3 offset1:1
	ds_write2_b32 v203, v4, v5 offset1:1
	ds_write2_b32 v204, v10, v11 offset1:1
	ds_write2_b32 v205, v12, v13 offset1:1
	ds_write2_b32 v206, v62, v63 offset1:1
	ds_write2_b32 v207, v64, v65 offset1:1
	s_waitcnt lgkmcnt(0)
	s_xor_b64 s[94:95], s[80:81], -1
	s_mov_b64 s[0:1], -1
	s_xor_b64 s[90:91], s[86:87], -1
	s_and_b64 vcc, exec, s[94:95]
	v_add_u32_e32 v177, s15, v153
	v_add_u32_e32 v172, 0x400, v155
	s_cbranch_vccz .LBB0_59
	ds_read2_b32 v[130:131], v155 offset1:65
	ds_read2_b32 v[132:133], v155 offset0:130 offset1:195
	s_waitcnt lgkmcnt(1)
	v_cvt_pk_bf16_f32 v130, v130, v131
	s_waitcnt lgkmcnt(0)
	v_cvt_pk_bf16_f32 v131, v132, v133
	ds_read2_b32 v[132:133], v172 offset0:4 offset1:69
	s_and_b64 vcc, exec, s[90:91]
	s_waitcnt lgkmcnt(0)
	v_cvt_pk_bf16_f32 v132, v132, v133
	ds_read2_b32 v[138:139], v172 offset0:134 offset1:199
	s_waitcnt lgkmcnt(0)
	v_cvt_pk_bf16_f32 v133, v138, v139
	s_cbranch_vccz .LBB0_28
	v_and_b32_e32 v142, 0x7f, v177
	s_mov_b64 s[0:1], 0
